# fp8 conversion slots rotated per XCD so concurrent converters read different column windows (cslot = (vcu + vcu/32) & 15), on top of nt loads + reversed P6
# baseline (speedup 1.0000x reference)
; #define LAS __attribute__((address_space(3)))
; __device__ __forceinline__ int fresh_lane() { unsigned z = 0u; asm volatile("" : "+v"(z)); return (int)__builtin_amdgcn_mbcnt_hi(~0u, __builtin_amdgcn_mbcnt_lo(~0u, z)); }
; __device__ __forceinline__ float shx(float v, int m, int lane) { return __int_as_float(__builtin_amdgcn_ds_bpermute((lane ^ m) << 2, __float_as_int(v))); }
; #define ATT_BAR() do { asm volatile("s_waitcnt lgkmcnt(0)" ::: "memory"); __builtin_amdgcn_s_barrier(); asm volatile("" ::: "memory"); } while (0)
; __device__ __forceinline__ void f8_share(const P& p, LAS unsigned char* ring, int G, int vcu, int wave) {
;     const int lane = fresh_lane(); LAS float* scr = (LAS float*)(ring + wave * 16384);
;     const int gw = vcu * NWAVES + wave, NGW = G * NWAVES; constexpr int NF8 = NE * (8 * 64 + 8 * 32);
;     f32x4 va[16], vb[16]; int it = gw;
;     F8Item ia = f8_item(p, it < NF8 ? it : 0), ib = ia;
;     if (it < NF8) f8_load(ia, va, lane);
;     if (it + NGW < NF8) { ib = f8_item(p, it + NGW); f8_load(ib, vb, lane); }
; __device__ __forceinline__ void phase(const P& p, LAS unsigned char* lds, int G, int vcu, const int wid) {
;     const int lane = fresh_lane();
;     const bf16_t* MT = (const bf16_t*)(p.ws + WS_META); bf16_t* MX = (bf16_t*)(p.ws + WS_MIXED);
;     float sa = lane < 32 ? p.lq1[lane] * p.lk1[lane] : 0.f, sb = lane < 32 ? p.lq2[lane] * p.lk2[lane] : 0.f;
; #pragma unroll
;     for (int o = 1; o < 64; o <<= 1) { sa += shx(sa, o, lane); sb += shx(sb, o, lane); }
;     const float lam = __expf(sa) - __expf(sb) + 0.2f;
;     const int cslot = vcu & 15; int iter = 0;
;     { LAS float* gdh = (LAS float*)(lds + GDH_OFF); if (wid == 0) gdh[lane] = p.g_dh[lane]; ATT_BAR(); }
;     bf16x8 qrd[4]; bool pred = false;
;     ...
;     for (int U = vcu; U < NB * 8 * 16; U += G) {
;         if (iter++ == cslot) { ATT_BAR(); f8_share(p, lds, G, vcu, wid); ATT_BAR(); }
;         ATT_DIFF_SRC(U, S, h, tok0, b);
;         const int Un = U + G; const bool pn = Un < NB * 8 * 16 && iter != cslot;
;         ATT_DIFF_SRC(pn ? Un : U, Sn, hn, tok0n, bn);
.LBB7_394:
	s_lshr_b32 s78, s95, 5
	s_add_i32 s78, s78, s95
	s_and_b32 s78, s78, 15
	s_add_u32 s79, s30, 0x3c0000
	s_addc_u32 s80, s31, 0
	s_add_u32 s0, s30, 0x37000000
	v_writelane_b32 v254, s0, 43
	s_addc_u32 s0, s31, 0
	v_writelane_b32 v254, s0, 42
	s_waitcnt lgkmcnt(0)
	s_barrier
	v_writelane_b32 v254, s92, 45
	s_cmpk_lt_i32 s95, 0x800
	v_writelane_b32 v254, s94, 48
	s_mov_b32 s83, 0
	s_cselect_b64 s[0:1], -1, 0
	s_cmpk_gt_i32 s95, 0x7ff
	s_mul_i32 s35, s94, 0xffffc400
	s_mul_i32 s53, s94, 0x1e00
	v_writelane_b32 v254, s95, 44
	s_cbranch_scc1 .LBB7_447
	v_writelane_b32 v254, s0, 49
	s_lshl_b32 s87, s95, 3
	s_add_i32 s87, s87, s94
	v_writelane_b32 v254, s1, 50
	s_lshl_b32 s0, s94, 14
	s_add_i32 s86, s0, 0
	s_lshl_b32 s88, s3, 3
	s_cmpk_lt_i32 s87, 0x6000
	s_cselect_b64 s[0:1], -1, 0
	v_cndmask_b32_e64 v163, 0, 1, s[0:1]
	s_and_b64 s[0:1], s[0:1], exec
	s_cselect_b32 s2, s87, 0
	s_lshl_b32 s4, s2, 2
	s_and_b32 s33, s4, 0x380
	s_lshl_b32 s4, s2, 5
	s_and_b32 s38, s4, 0x3e0
	s_ashr_i32 s4, s2, 31
	s_lshr_b32 s4, s4, 23
	s_add_i32 s5, s2, s4
	s_ashr_i32 s4, s5, 9
	s_and_b32 s5, s5, 0xfe00
	s_sub_i32 s12, s2, s5
	s_ashr_i32 s5, s4, 31
	s_lshl_b64 s[6:7], s[4:5], 23
	s_lshl_b64 s[10:11], s[4:5], 21
	s_sext_i32_i16 s4, s12
	s_bfe_u32 s4, s4, 0x60019
	s_add_i32 s4, s12, s4
	s_sext_i32_i16 s5, s4
	s_and_b32 s4, s4, 0xffc0
	s_add_i32 s0, s2, 0xffffc000
	s_sub_i32 s4, s12, s4
	s_mov_b32 s9, 0
	s_lshr_b32 s8, s0, 8
	s_lshl_b32 s5, s5, 1
	s_sext_i32_i16 s4, s4
	s_lshl_b64 s[0:1], s[8:9], 20
	s_and_b32 s39, s5, 0xffffff80
	s_lshl_b32 s40, s4, 5
	s_add_i32 s41, s87, s88
	s_cmpk_lt_i32 s41, 0x6000
	s_cselect_b64 s[70:71], -1, 0
	s_lshl_b32 s12, s41, 2
	s_and_b32 s42, s12, 0x380
	s_lshl_b32 s12, s41, 5
	s_and_b32 s43, s12, 0x3e0
	s_ashr_i32 s12, s41, 31
	s_lshr_b32 s12, s12, 23
	s_add_i32 s13, s41, s12
	s_ashr_i32 s12, s13, 9
	s_and_b32 s13, s13, 0xfe00
	s_sub_i32 s34, s41, s13
	s_ashr_i32 s13, s12, 31
	s_lshl_b64 s[16:17], s[12:13], 23
	s_lshl_b64 s[36:37], s[12:13], 21
	s_sext_i32_i16 s12, s34
	s_bfe_u32 s12, s12, 0x60019
	s_add_i32 s12, s34, s12
	s_sext_i32_i16 s13, s12
	s_and_b32 s12, s12, 0xffc0
	s_sub_i32 s12, s34, s12
	s_sext_i32_i16 s12, s12
	s_add_i32 s4, s41, 0xffffc000
	s_lshl_b32 s45, s12, 5
	s_lshl_b32 s12, s94, 8
	s_lshr_b32 s4, s4, 8
	s_mov_b32 s5, s9
	s_lshl_b32 s13, s13, 1
	s_add_i32 s91, s86, s35
	s_add_i32 s97, s12, 0
	s_lshl_b64 s[14:15], s[4:5], 20
	s_and_b32 s44, s13, 0xffffff80
	s_lshl_b32 s89, s3, 4
	s_lshl_b32 s90, s94, 5
	s_lshl_b32 s46, s94, 10
	s_add_i32 s97, s97, 0x1d000
	s_add_i32 s93, s91, s53
	s_lshl_b64 s[12:13], s[8:9], 22
	s_add_u32 s8, s24, s12
	s_addc_u32 s47, s25, s13
	s_add_u32 s48, s20, s6
	s_addc_u32 s49, s21, s7
	s_lshl_b64 s[4:5], s[4:5], 22
	s_add_u32 s50, s24, s4
	s_addc_u32 s51, s25, s5
	v_writelane_b32 v254, s35, 51
	s_add_u32 s52, s20, s16
	v_writelane_b32 v254, s53, 52
	s_addc_u32 s53, s21, s17
	s_add_u32 s68, s30, 0x2000000
	s_addc_u32 s69, s31, 0
	s_add_u32 s84, s30, 0x27000000
	s_addc_u32 s85, s31, 0
	s_add_u32 s34, s30, 0xc000000
	s_addc_u32 s35, s31, 0
	s_add_u32 s6, s30, 0x10000000
	s_addc_u32 s7, s31, 0
	s_add_u32 s92, s30, 0x14000000
	s_addc_u32 s4, s31, 0
	s_cmpk_lt_i32 s2, 0x4000
	s_cselect_b64 s[12:13], -1, 0
	s_mov_b32 s2, 0x27000000
	v_cndmask_b32_e64 v164, 0, 1, s[12:13]
	s_and_b64 s[12:13], s[12:13], exec
	s_cselect_b32 s13, s2, 0x2000000
	s_cselect_b32 s1, s11, s1
	s_cselect_b32 s0, s10, s0
	s_cselect_b32 s5, s39, s33
	s_cselect_b32 s12, s40, s38
	s_cselect_b32 s10, s49, s47
	s_cselect_b32 s8, s48, s8
	s_cselect_b32 s33, 11, 10
	s_add_u32 s11, s30, s13
	s_addc_u32 s13, s31, 0
	s_add_u32 s0, s11, s0
	s_addc_u32 s1, s13, s1
	v_writelane_b32 v254, s0, 53
	s_ashr_i32 s13, s12, 31
	s_waitcnt lgkmcnt(1)
	v_add_f32_e32 v0, v2, v4
	v_writelane_b32 v254, s1, 54
	s_lshl_b64 s[0:1], s[12:13], 2
	s_add_u32 s38, s8, s0
	s_addc_u32 s39, s10, s1
	s_or_b32 s0, s5, 32
	v_writelane_b32 v254, s0, 55
	s_or_b32 s0, s5, 33
	v_writelane_b32 v254, s0, 56
	s_or_b32 s0, s5, 34
	v_writelane_b32 v254, s0, 58
	s_or_b32 s0, s5, 0x41
	v_writelane_b32 v254, s0, 59
	s_or_b32 s0, s5, 0x42
	v_writelane_b32 v254, s0, 61
	s_or_b32 s0, s5, 0x61
	s_or_b32 s82, s5, 64
	s_or_b32 s81, s5, 0x60
	v_writelane_b32 v254, s0, 62
	s_or_b32 s0, s5, 0x62
	s_cmpk_lt_i32 s41, 0x4000
	v_writelane_b32 v254, s0, 63
	s_cselect_b64 s[0:1], -1, 0
	v_cndmask_b32_e64 v165, 0, 1, s[0:1]
	s_and_b64 s[0:1], s[0:1], exec
	s_cselect_b32 s0, s2, 0x2000000
	s_cselect_b32 s1, s37, s15
	s_cselect_b32 s2, s36, s14
	s_cselect_b32 s10, s53, s51
	s_cselect_b32 s11, s52, s50
	s_cselect_b32 s67, s44, s42
	s_cselect_b32 s14, s45, s43
	s_cselect_b32 s52, 11, 10
	s_add_u32 s0, s30, s0
	s_addc_u32 s13, s31, 0
	s_add_u32 s0, s0, s2
	s_waitcnt lgkmcnt(0)
	v_add_f32_e32 v1, v3, v5
	s_addc_u32 s1, s13, s1
	v_mul_f32_e32 v0, 0x3fb8aa3b, v0
	v_mul_f32_e32 v1, 0x3fb8aa3b, v1
	v_writelane_b32 v255, s0, 0
	v_exp_f32_e32 v0, v0
	v_exp_f32_e32 v1, v1
	v_writelane_b32 v255, s1, 1
	s_mov_b32 s0, s14
	s_ashr_i32 s15, s14, 31
	v_writelane_b32 v255, s0, 2
	s_mul_i32 s8, s94, 0xffffe200
	v_sub_f32_e32 v0, v0, v1
	v_writelane_b32 v255, s1, 3
	s_lshl_b64 s[0:1], s[14:15], 2
	s_add_u32 s44, s11, s0
	s_addc_u32 s45, s10, s1
	s_add_i32 s96, s93, s8
	v_add_f32_e32 v162, 0x3e4ccccd, v0
	s_add_i32 s41, s46, 0
	v_mov_b32_e32 v166, 0
	s_mov_b64 s[54:55], 0
	v_mov_b32_e32 v157, 0
	s_mov_b32 s66, 0xc3e00000
	s_movk_i32 s14, 0x7f
	s_add_i32 s15, s91, 0x2000
	s_mov_b64 s[46:47], 0x2000
	s_mov_b64 s[48:49], 0x4000
	s_add_i32 s42, s96, 0xa000
	s_mov_b64 s[50:51], 0x6000
	s_add_i32 s43, s96, 0xe000
	s_movk_i32 s40, 0x110
	v_mov_b32_e32 v167, 0x3727c5ac
	v_mov_b32_e32 v168, 0x43e00000
	v_mov_b32_e32 v178, 0
	v_mov_b32_e32 v177, 0
	v_mov_b32_e32 v176, 0
	v_mov_b32_e32 v175, 0
	v_mov_b32_e32 v174, 0
	v_mov_b32_e32 v173, 0
	v_mov_b32_e32 v172, 0
	v_mov_b32_e32 v161, 0
	v_mov_b32_e32 v160, 0
	v_mov_b32_e32 v155, 0
	v_mov_b32_e32 v154, 0
	v_mov_b32_e32 v153, 0
	v_mov_b32_e32 v152, 0
	v_mov_b32_e32 v151, 0
	v_mov_b32_e32 v150, 0
	v_mov_b32_e32 v145, 0
	s_cmp_lg_u32 s83, s78
	s_cbranch_scc1 .LBB7_433
	s_branch .LBB7_399
